# v10 + conversion windows re-sized: prologue 736 MoE items, A 9/wave, B 6, C 2 (idle ctx-set workgroups only), D 7, E 6; all conversions finish before layer 3
# speedup vs baseline: 1.0098x; 1.0021x over previous
.LBB0_15:
	s_load_dwordx16 s[4:19], s[0:1], 0x0
	s_waitcnt lgkmcnt(0)
	v_writelane_b32 v253, s4, 34
	s_nop 1
	v_writelane_b32 v253, s5, 35
	v_writelane_b32 v253, s6, 36
	v_writelane_b32 v253, s7, 37
	v_writelane_b32 v253, s8, 38
	v_writelane_b32 v253, s9, 39
	v_writelane_b32 v253, s10, 40
	v_writelane_b32 v253, s11, 41
	v_writelane_b32 v253, s12, 42
	v_writelane_b32 v253, s13, 43
	v_writelane_b32 v253, s14, 44
	v_writelane_b32 v253, s15, 45
	v_writelane_b32 v253, s16, 46
	v_writelane_b32 v253, s17, 47
	v_writelane_b32 v253, s18, 48
	v_writelane_b32 v253, s19, 49
	s_load_dwordx16 s[4:19], s[0:1], 0x40
	s_lshr_b32 s0, s33, 6
	s_waitcnt lgkmcnt(0)
	v_writelane_b32 v253, s4, 50
	s_nop 1
	v_writelane_b32 v253, s5, 51
	v_writelane_b32 v253, s6, 52
	v_writelane_b32 v253, s7, 53
	v_writelane_b32 v253, s8, 54
	v_writelane_b32 v253, s9, 55
	v_writelane_b32 v253, s10, 56
	v_writelane_b32 v253, s11, 57
	v_writelane_b32 v253, s12, 58
	v_writelane_b32 v253, s13, 59
	v_writelane_b32 v253, s14, 60
	v_writelane_b32 v253, s15, 61
	v_writelane_b32 v253, s16, 62
	v_writelane_b32 v254, s18, 0
	v_writelane_b32 v253, s17, 63
	v_writelane_b32 v254, s19, 1
	v_writelane_b32 v254, s0, 2
	v_readlane_b32 s0, v253, 4
	v_readlane_b32 s1, v253, 5
	s_mov_b64 s[4:5], s[0:1]
	s_cmp_gt_i32 s4, 0
	v_readlane_b32 s2, v253, 6
	v_readlane_b32 s3, v253, 7
	s_cselect_b64 s[0:1], -1, 0
	s_cmp_lt_i32 s5, 1
	s_cselect_b64 s[2:3], -1, 0
	s_or_b64 s[0:1], s[0:1], s[2:3]
	s_and_b64 vcc, exec, s[0:1]
	s_cbranch_vccnz .LBB0_143
	v_readlane_b32 s0, v253, 3
	s_lshl_b32 s0, s0, 3
	v_readlane_b32 s1, v254, 2
	s_add_i32 s14, s0, s1
	s_lshl_b32 s15, s70, 3
	s_cmpk_eq_i32 s70, 0x100
	s_movk_i32 s0, 0x2000
	s_cselect_b32 s16, s0, 0x19d20
	v_readlane_b32 s0, v253, 8
	v_readlane_b32 s2, v253, 10
	v_readlane_b32 s3, v253, 11
	v_readlane_b32 s6, v253, 14
	v_readlane_b32 s7, v253, 15
	s_mov_b64 s[2:3], s[6:7]
	s_cmp_ge_i32 s14, s16
	v_mbcnt_lo_u32_b32 v1, -1, 0
	v_mbcnt_hi_u32_b32 v1, -1, v1
	v_readlane_b32 s1, v253, 9
	v_and_b32_e32 v0, 63, v1
	v_readlane_b32 s4, v253, 12
	v_readlane_b32 s5, v253, 13
	s_cbranch_scc1 .LBB0_38
	v_readlane_b32 s0, v254, 2
	s_lshl_b32 s0, s0, 14
	s_add_i32 s0, s0, 0
	s_add_u32 s17, s2, 0x31a00000
	s_addc_u32 s18, s3, 0
	s_add_u32 s19, s2, 0x21a00000
	s_addc_u32 s20, s3, 0
	s_add_u32 s21, s2, 0x21600000
	s_addc_u32 s22, s3, 0
	s_add_u32 s23, s2, 0x20900000
	s_addc_u32 s24, s3, 0
	v_lshrrev_b32_e32 v24, 3, v0
	v_and_b32_e32 v4, 7, v1
	s_add_u32 s25, s2, 0x20500000
	v_lshlrev_b32_e32 v14, 10, v24
	v_lshl_add_u32 v5, v4, 4, s0
	v_mul_u32_u24_e32 v6, 0x84, v24
	s_addc_u32 s26, s3, 0
	v_lshlrev_b32_e32 v2, 2, v4
	v_or_b32_e32 v16, 0x2000, v14
	v_or_b32_e32 v18, 0x4000, v14
	v_or_b32_e32 v20, 0x6000, v14
	v_lshlrev_b32_e32 v12, 3, v4
	v_mul_u32_u24_e32 v4, 0x420, v4
	v_lshlrev_b32_e32 v7, 2, v24
	s_add_u32 s27, s2, 0x1fc00000
	v_add_u32_e32 v26, v5, v6
	s_mov_b32 s1, 0
	v_mov_b32_e32 v3, 0
	v_add3_u32 v25, s0, v4, v7
	s_addc_u32 s28, s3, 0
	s_mov_b32 s29, 0x30000
	v_add_u32_e32 v27, 0x420, v26
	v_add_u32_e32 v28, 0x428, v26
	v_add_u32_e32 v29, 0x840, v26
	v_add_u32_e32 v30, 0x848, v26
	v_add_u32_e32 v31, 0xc60, v26
	v_add_u32_e32 v32, 0xc68, v26
	v_add_u32_e32 v33, 0x1080, v26
	v_add_u32_e32 v34, 0x1088, v26
	v_add_u32_e32 v35, 0x14a0, v26
	v_add_u32_e32 v36, 0x14a8, v26
	v_add_u32_e32 v37, 0x18c0, v26
	v_add_u32_e32 v38, 0x18c8, v26
	v_add_u32_e32 v39, 0x1ce0, v26
	v_add_u32_e32 v40, 0x1ce8, v26
	s_movk_i32 s30, 0x7fff
	s_mov_b32 s31, 0xffff0000
	s_movk_i32 s34, 0x2400
	v_lshlrev_b32_e32 v2, 2, v2
	v_lshlrev_b32_e32 v4, 2, v14
	v_lshlrev_b32_e32 v6, 2, v16
	v_lshlrev_b32_e32 v8, 2, v18
	v_lshlrev_b32_e32 v10, 2, v20
	v_lshlrev_b32_e32 v12, 1, v12
	v_lshlrev_b32_e32 v14, 1, v14
	v_lshlrev_b32_e32 v16, 1, v16
	v_lshlrev_b32_e32 v18, 1, v18
	v_lshlrev_b32_e32 v20, 1, v20
	s_mov_b32 s35, s14
	s_branch .LBB0_19

.LBB0_322:
	s_cmpk_gt_i32 s3, 0xe7
	v_readlane_b32 s2, v254, 39
	s_cselect_b64 s[0:1], -1, 0
	v_readlane_b32 s3, v254, 40
	s_and_b64 s[0:1], s[2:3], s[0:1]
	s_andn2_b64 vcc, exec, s[0:1]
	s_cbranch_vccnz .LBB0_336
	v_readlane_b32 s2, v254, 59
	s_cmp_eq_u32 s2, 0
	s_mov_b32 s0, 0x84a0
	s_cselect_b32 s0, 0x2e0, s0
	s_cmp_gt_u32 s2, 1
	s_cselect_b32 s1, 0x78c0, 0
	s_add_i32 s0, s0, s1
	s_cmp_eq_u32 s2, 3
	s_cselect_b32 s1, 0x81c0, 0
	s_add_i32 s2, s0, s1
	v_readlane_b32 s0, v255, 0
	s_mul_i32 s3, s0, 72
	s_add_i32 s16, s2, 0x6c0
	s_min_u32 s16, s16, 0x18000
	s_add_i32 s2, s2, s56
	v_readlane_b32 s4, v253, 8
	s_add_i32 s14, s2, s3
	v_readlane_b32 s10, v253, 14
	v_readlane_b32 s11, v253, 15
	s_add_i32 s14, s14, 0xffffbec0
	s_mov_b64 s[0:1], s[10:11]
	s_cmp_ge_i32 s14, s16
	v_readlane_b32 s5, v253, 9
	v_readlane_b32 s6, v253, 10
	v_readlane_b32 s7, v253, 11
	v_readlane_b32 s8, v253, 12
	v_readlane_b32 s9, v253, 13
	v_mbcnt_lo_u32_b32 v0, -1, 0
	v_mbcnt_hi_u32_b32 v0, -1, v0
	s_cbranch_scc1 .LBB0_336
	s_mul_hi_i32 s2, s14, 0x2aaaaaab
	s_lshr_b32 s3, s2, 31
	s_ashr_i32 s2, s2, 12
	s_add_i32 s3, s2, s3
	s_mul_i32 s2, s3, 0x6000
	s_sub_i32 s19, s14, s2
	s_lshl_b32 s15, s19, 5
	s_lshl_b32 s3, s3, 4
	s_bfe_u32 s4, s19, 0x40009
	s_bfe_u32 s18, s19, 0x40005
	s_and_b32 s2, s15, 0x3e0
	s_ashr_i32 s17, s19, 13
	s_or_b32 s8, s4, s3
	s_cmp_gt_i32 s17, 1
	s_mov_b64 s[12:13], -1
	s_cbranch_scc0 .LBB0_326
	s_ashr_i32 s9, s8, 31
	v_readlane_b32 s20, v253, 8
	s_lshl_b64 s[4:5], s[8:9], 22
	v_readlane_b32 s22, v253, 10
	v_readlane_b32 s23, v253, 11
	s_add_u32 s3, s22, s4
	s_addc_u32 s4, s23, s5
	s_lshl_b32 s30, s18, 6
	s_lshl_b32 s5, s18, 18
	s_add_u32 s5, s3, s5
	s_addc_u32 s4, s4, 0
	s_lshl_b32 s6, s2, 2
	s_add_u32 s6, s5, s6
	s_addc_u32 s7, s4, 0
	s_lshl_b64 s[4:5], s[8:9], 21
	s_add_u32 s4, s0, s4
	s_addc_u32 s5, s1, s5
	s_add_u32 s4, s4, 0x31a00000
	v_readlane_b32 s21, v253, 9
	v_readlane_b32 s24, v253, 12
	v_readlane_b32 s25, v253, 13
	v_readlane_b32 s26, v253, 14
	v_readlane_b32 s27, v253, 15
	s_mov_b32 s3, s31
	s_addc_u32 s5, s5, 0
	s_mov_b64 s[12:13], 0

.LBB0_331:
	s_cmp_gt_u32 s17, 7
	s_cselect_b64 s[0:1], -1, 0
	s_cmp_ge_i32 s22, s16
	s_cselect_b64 s[6:7], -1, 0
	s_or_b64 s[0:1], s[0:1], s[6:7]
	s_and_b64 vcc, exec, s[0:1]
	s_cbranch_vccnz .LBB0_330
	s_mul_hi_i32 s2, s22, 0x2aaaaaab
	s_lshr_b32 s3, s2, 31
	s_ashr_i32 s2, s2, 12
	s_add_i32 s3, s2, s3
	s_mul_i32 s2, s3, 0xffffa000
	s_add_i32 s27, s22, s2
	s_mul_i32 s2, s3, 0xfff40000
	s_add_i32 s24, s23, s2
	s_lshl_b32 s3, s3, 4
	s_bfe_u32 s6, s27, 0x40009
	s_bfe_u32 s26, s27, 0x40005
	s_and_b32 s2, s24, 0x3e0
	s_ashr_i32 s25, s27, 13
	s_or_b32 s12, s6, s3
	s_cmp_gt_i32 s25, 1
	s_mov_b64 s[14:15], -1
	s_cbranch_scc0 .LBB0_334
	s_ashr_i32 s13, s12, 31
	v_readlane_b32 s36, v253, 8
	s_lshl_b64 s[6:7], s[12:13], 22
	v_readlane_b32 s38, v253, 10
	v_readlane_b32 s39, v253, 11
	s_add_u32 s3, s38, s6
	s_addc_u32 s6, s39, s7
	s_lshl_b32 s30, s26, 6
	s_lshl_b32 s7, s26, 18
	s_add_u32 s7, s3, s7
	s_addc_u32 s6, s6, 0
	s_lshl_b32 s8, s2, 2
	s_add_u32 s8, s7, s8
	s_addc_u32 s9, s6, 0
	s_lshl_b64 s[6:7], s[12:13], 21
	v_readlane_b32 s42, v253, 14
	v_readlane_b32 s43, v253, 15
	s_add_u32 s6, s18, s6
	v_readlane_b32 s37, v253, 9
	v_readlane_b32 s40, v253, 12
	v_readlane_b32 s41, v253, 13
	s_mov_b32 s43, 0x17401000
	s_mov_b32 s42, 0x13001000
	s_mov_b32 s3, s31
	s_addc_u32 s7, s19, s7
	s_mov_b64 s[14:15], 0

.LBB0_658:
	v_readlane_b32 s0, v255, 0
	s_cmpk_gt_i32 s0, 0xc7
	v_readlane_b32 s2, v254, 39
	s_cselect_b64 s[0:1], -1, 0
	v_readlane_b32 s3, v254, 40
	s_and_b64 s[0:1], s[2:3], s[0:1]
	s_andn2_b64 vcc, exec, s[0:1]
	s_cbranch_vccnz .LBB0_672
	v_readlane_b32 s1, v254, 59
	s_cmp_eq_u32 s1, 0
	s_mov_b32 s0, 0x84a0
	s_cselect_b32 s0, 0x2e0, s0
	s_cmp_gt_u32 s1, 1
	s_cselect_b32 s1, 0x78c0, 0
	s_add_i32 s8, s0, s1
	v_readlane_b32 s0, v255, 0
	v_readlane_b32 s12, v253, 8
	s_mul_i32 s2, s0, 72
	v_readlane_b32 s14, v253, 10
	s_add_i32 s3, s8, s56
	s_add_i32 s14, s3, s2
	v_readlane_b32 s18, v253, 14
	v_readlane_b32 s19, v253, 15
	s_add_i32 s14, s14, 0xffffc7c0
	s_add_i32 s8, s8, 0xfc0
	s_min_u32 s8, s8, 0x18000
	s_mov_b64 s[0:1], s[18:19]
	s_cmp_ge_i32 s14, s8
	v_readlane_b32 s13, v253, 9
	v_readlane_b32 s15, v253, 11
	v_readlane_b32 s16, v253, 12
	v_readlane_b32 s17, v253, 13
	v_mbcnt_lo_u32_b32 v0, -1, 0
	v_mbcnt_hi_u32_b32 v0, -1, v0
	s_cbranch_scc1 .LBB0_672
	s_mul_hi_i32 s2, s14, 0x2aaaaaab
	s_lshr_b32 s3, s2, 31
	s_ashr_i32 s2, s2, 12
	s_add_i32 s3, s2, s3
	s_mul_i32 s2, s3, 0x6000
	s_sub_i32 s17, s14, s2
	s_lshl_b32 s9, s17, 5
	s_lshl_b32 s3, s3, 4
	s_bfe_u32 s4, s17, 0x40009
	s_bfe_u32 s16, s17, 0x40005
	s_and_b32 s2, s9, 0x3e0
	s_ashr_i32 s15, s17, 13
	s_or_b32 s10, s4, s3
	s_cmp_gt_i32 s15, 1
	s_mov_b64 s[12:13], -1
	s_cbranch_scc0 .LBB0_662
	s_ashr_i32 s11, s10, 31
	v_readlane_b32 s20, v253, 8
	s_lshl_b64 s[4:5], s[10:11], 22
	v_readlane_b32 s22, v253, 10
	v_readlane_b32 s23, v253, 11
	s_add_u32 s3, s22, s4
	s_addc_u32 s4, s23, s5
	s_lshl_b32 s30, s16, 6
	s_lshl_b32 s5, s16, 18
	s_add_u32 s5, s3, s5
	s_addc_u32 s4, s4, 0
	s_lshl_b32 s6, s2, 2
	s_add_u32 s6, s5, s6
	s_addc_u32 s7, s4, 0
	s_lshl_b64 s[4:5], s[10:11], 21
	s_add_u32 s4, s0, s4
	s_addc_u32 s5, s1, s5
	s_add_u32 s4, s4, 0x31a00000
	v_readlane_b32 s21, v253, 9
	v_readlane_b32 s24, v253, 12
	v_readlane_b32 s25, v253, 13
	v_readlane_b32 s26, v253, 14
	v_readlane_b32 s27, v253, 15
	s_mov_b32 s3, s31
	s_addc_u32 s5, s5, 0
	s_mov_b64 s[12:13], 0

.LBB0_667:
	s_cmp_gt_u32 s9, 7
	s_cselect_b64 s[0:1], -1, 0
	s_cmp_ge_i32 s20, s8
	s_cselect_b64 s[6:7], -1, 0
	s_or_b64 s[0:1], s[0:1], s[6:7]
	s_and_b64 vcc, exec, s[0:1]
	s_cbranch_vccnz .LBB0_666
	s_mul_hi_i32 s2, s20, 0x2aaaaaab
	s_lshr_b32 s3, s2, 31
	s_ashr_i32 s2, s2, 12
	s_add_i32 s3, s2, s3
	s_mul_i32 s2, s3, 0xffffa000
	s_add_i32 s25, s20, s2
	s_mul_i32 s2, s3, 0xfff40000
	s_add_i32 s22, s21, s2
	s_lshl_b32 s3, s3, 4
	s_bfe_u32 s6, s25, 0x40009
	s_bfe_u32 s24, s25, 0x40005
	s_and_b32 s2, s22, 0x3e0
	s_ashr_i32 s23, s25, 13
	s_or_b32 s12, s6, s3
	s_cmp_gt_i32 s23, 1
	s_mov_b64 s[14:15], -1
	s_cbranch_scc0 .LBB0_670
	s_ashr_i32 s13, s12, 31
	v_readlane_b32 s36, v253, 8
	s_lshl_b64 s[6:7], s[12:13], 22
	v_readlane_b32 s38, v253, 10
	v_readlane_b32 s39, v253, 11
	s_add_u32 s3, s38, s6
	s_addc_u32 s6, s39, s7
	s_lshl_b32 s30, s24, 6
	s_lshl_b32 s7, s24, 18
	s_add_u32 s7, s3, s7
	s_addc_u32 s6, s6, 0
	s_lshl_b32 s10, s2, 2
	s_add_u32 s10, s7, s10
	s_addc_u32 s11, s6, 0
	s_lshl_b64 s[6:7], s[12:13], 21
	v_readlane_b32 s42, v253, 14
	v_readlane_b32 s43, v253, 15
	s_add_u32 s6, s16, s6
	v_readlane_b32 s37, v253, 9
	v_readlane_b32 s40, v253, 12
	v_readlane_b32 s41, v253, 13
	s_mov_b32 s43, 0x17401000
	s_mov_b32 s42, 0x13001000
	s_mov_b32 s3, s31
	s_addc_u32 s7, s17, s7
	s_mov_b64 s[14:15], 0

.LBB0_1122:
	v_readlane_b32 s0, v254, 59
	s_cmp_lg_u32 s0, 3
	v_readlane_b32 s2, v254, 39
	s_cselect_b64 s[0:1], -1, 0
	v_readlane_b32 s3, v254, 40
	s_and_b64 s[0:1], s[2:3], s[0:1]
	s_cmp_gt_i32 s6, 31
	s_cselect_b64 s[2:3], -1, 0
	s_and_b64 s[0:1], s[0:1], s[2:3]
	s_andn2_b64 vcc, exec, s[0:1]
	s_cbranch_vccnz .LBB0_1136
	v_readlane_b32 s0, v255, 1
	v_readlane_b32 s1, v255, 2
	s_and_b64 s[0:1], s[0:1], exec
	s_movk_i32 s0, 0xfc0
	v_readlane_b32 s2, v254, 59
	s_cselect_b32 s0, s0, 0x6c0
	s_cmp_eq_u32 s2, 0
	s_mov_b32 s1, 0x84a0
	s_cselect_b32 s1, 0x2e0, s1
	s_cmp_gt_u32 s2, 1
	s_cselect_b32 s2, 0x78c0, 0
	s_add_i32 s1, s1, s2
	s_add_i32 s14, s1, s0
	v_readlane_b32 s0, v255, 0
	s_mul_i32 s2, s0, 48
	s_add_i32 s3, s14, s56
	v_readlane_b32 s4, v253, 8
	s_add_i32 s12, s3, s2
	v_readlane_b32 s10, v253, 14
	v_readlane_b32 s11, v253, 15
	s_add_i32 s12, s12, 0xfffffa00
	s_add_i32 s14, s14, 0x2a00
	s_min_u32 s14, s14, 0x18000
	s_mov_b64 s[0:1], s[10:11]
	s_cmp_ge_i32 s12, s14
	v_readlane_b32 s5, v253, 9
	v_readlane_b32 s6, v253, 10
	v_readlane_b32 s7, v253, 11
	v_readlane_b32 s8, v253, 12
	v_readlane_b32 s9, v253, 13
	v_mbcnt_lo_u32_b32 v0, -1, 0
	v_mbcnt_hi_u32_b32 v0, -1, v0
	s_cbranch_scc1 .LBB0_1136
	s_mul_hi_i32 s2, s12, 0x2aaaaaab
	s_lshr_b32 s3, s2, 31
	s_ashr_i32 s2, s2, 12
	s_add_i32 s3, s2, s3
	s_mul_i32 s2, s3, 0x6000
	s_sub_i32 s17, s12, s2
	s_lshl_b32 s13, s17, 5
	s_lshl_b32 s3, s3, 4
	s_bfe_u32 s4, s17, 0x40009
	s_bfe_u32 s16, s17, 0x40005
	s_and_b32 s2, s13, 0x3e0
	s_ashr_i32 s15, s17, 13
	s_or_b32 s8, s4, s3
	s_cmp_gt_i32 s15, 1
	s_mov_b64 s[10:11], -1
	s_cbranch_scc0 .LBB0_1126
	s_ashr_i32 s9, s8, 31
	v_readlane_b32 s20, v253, 8
	s_lshl_b64 s[4:5], s[8:9], 22
	v_readlane_b32 s22, v253, 10
	v_readlane_b32 s23, v253, 11
	s_add_u32 s3, s22, s4
	s_addc_u32 s4, s23, s5
	s_lshl_b32 s30, s16, 6
	s_lshl_b32 s5, s16, 18
	s_add_u32 s5, s3, s5
	s_addc_u32 s4, s4, 0
	s_lshl_b32 s6, s2, 2
	s_add_u32 s6, s5, s6
	s_addc_u32 s7, s4, 0
	s_lshl_b64 s[4:5], s[8:9], 21
	s_add_u32 s4, s0, s4
	s_addc_u32 s5, s1, s5
	s_add_u32 s4, s4, 0x31a00000
	v_readlane_b32 s21, v253, 9
	v_readlane_b32 s24, v253, 12
	v_readlane_b32 s25, v253, 13
	v_readlane_b32 s26, v253, 14
	v_readlane_b32 s27, v253, 15
	s_mov_b32 s3, s31
	s_addc_u32 s5, s5, 0
	s_mov_b64 s[10:11], 0

.LBB0_1131:
	s_cmp_gt_u32 s15, 4
	s_cselect_b64 s[0:1], -1, 0
	s_cmp_ge_i32 s20, s14
	s_cselect_b64 s[6:7], -1, 0
	s_or_b64 s[0:1], s[0:1], s[6:7]
	s_and_b64 vcc, exec, s[0:1]
	s_cbranch_vccnz .LBB0_1130
	s_mul_hi_i32 s2, s20, 0x2aaaaaab
	s_lshr_b32 s3, s2, 31
	s_ashr_i32 s2, s2, 12
	s_add_i32 s3, s2, s3
	s_mul_i32 s2, s3, 0xffffa000
	s_add_i32 s25, s20, s2
	s_mul_i32 s2, s3, 0xfff40000
	s_add_i32 s22, s21, s2
	s_lshl_b32 s3, s3, 4
	s_bfe_u32 s6, s25, 0x40009
	s_bfe_u32 s24, s25, 0x40005
	s_and_b32 s2, s22, 0x3e0
	s_ashr_i32 s23, s25, 13
	s_or_b32 s10, s6, s3
	s_cmp_gt_i32 s23, 1
	s_mov_b64 s[12:13], -1
	s_cbranch_scc0 .LBB0_1134
	s_ashr_i32 s11, s10, 31
	v_readlane_b32 s36, v253, 8
	s_lshl_b64 s[6:7], s[10:11], 22
	v_readlane_b32 s38, v253, 10
	v_readlane_b32 s39, v253, 11
	s_add_u32 s3, s38, s6
	s_addc_u32 s6, s39, s7
	s_lshl_b32 s30, s24, 6
	s_lshl_b32 s7, s24, 18
	s_add_u32 s7, s3, s7
	s_addc_u32 s6, s6, 0
	s_lshl_b32 s8, s2, 2
	s_add_u32 s8, s7, s8
	s_addc_u32 s9, s6, 0
	s_lshl_b64 s[6:7], s[10:11], 21
	v_readlane_b32 s42, v253, 14
	v_readlane_b32 s43, v253, 15
	s_add_u32 s6, s16, s6
	v_readlane_b32 s37, v253, 9
	v_readlane_b32 s40, v253, 12
	v_readlane_b32 s41, v253, 13
	s_mov_b32 s43, 0x17401000
	s_mov_b32 s42, 0x13001000
	s_mov_b32 s3, s31
	s_addc_u32 s7, s17, s7
	s_mov_b64 s[12:13], 0

.LBB0_1347:
	v_readlane_b32 s4, v254, 61
	s_cmpk_gt_i32 s4, 0x7f
	v_readlane_b32 s2, v254, 39
	s_cselect_b64 s[0:1], -1, 0
	v_readlane_b32 s3, v254, 40
	s_and_b64 s[0:1], s[2:3], s[0:1]
	s_andn2_b64 vcc, exec, s[0:1]
	s_mov_b32 s29, 0xffff0000
	s_movk_i32 s33, 0x7fff
	v_readlane_b32 s56, v255, 7
	s_cbranch_vccnz .LBB0_1361
	v_readlane_b32 s0, v255, 1
	v_readlane_b32 s1, v255, 2
	s_and_b64 s[0:1], s[0:1], exec
	s_movk_i32 s0, 0xfc0
	v_readlane_b32 s1, v254, 59
	s_cselect_b32 s2, s0, 0x6c0
	s_cmp_eq_u32 s1, 0
	s_mov_b32 s0, 0x84a0
	s_cselect_b32 s0, 0x2e0, s0
	s_cmp_gt_u32 s1, 1
	s_cselect_b32 s1, 0x78c0, 0
	v_readlane_b32 s6, v255, 3
	s_add_i32 s3, s0, s1
	v_readlane_b32 s7, v255, 4
	s_and_b64 s[0:1], s[6:7], exec
	s_cselect_b32 s0, 0x81c0, 0
	s_add_i32 s3, s3, s0
	s_and_b64 s[0:1], s[6:7], exec
	s_cselect_b32 s0, 0, 0x2a00
	s_add_i32 s0, s3, s0
	s_add_i32 s2, s0, s2
	s_cmpk_gt_i32 s4, 0x7f
	s_cselect_b32 s100, 1, 1
	s_cselect_b32 s3, 16, 16
	s_mov_b32 s101, 0xfffff800
	s_cselect_b32 s101, 0xfffff800, s101
	s_mul_i32 s3, s4, s3
	s_add_i32 s3, s3, s101
	v_readlane_b32 s4, v253, 8
	s_add_i32 s4, s2, s56
	s_add_i32 s12, s4, s3
	s_min_u32 s14, s2, 0x17800
	v_readlane_b32 s10, v253, 14
	v_readlane_b32 s11, v253, 15
	s_nop 0
	s_add_i32 s14, s14, 0x800
	s_mov_b64 s[0:1], s[10:11]
	s_cmp_ge_i32 s12, s14
	v_readlane_b32 s5, v253, 9
	v_readlane_b32 s6, v253, 10
	v_readlane_b32 s7, v253, 11
	v_readlane_b32 s8, v253, 12
	v_readlane_b32 s9, v253, 13
	v_mbcnt_lo_u32_b32 v0, -1, 0
	v_mbcnt_hi_u32_b32 v0, -1, v0
	s_cbranch_scc1 .LBB0_1361
	s_mul_hi_i32 s2, s12, 0x2aaaaaab
	s_lshr_b32 s3, s2, 31
	s_ashr_i32 s2, s2, 12
	s_add_i32 s3, s2, s3
	s_mul_i32 s2, s3, 0x6000
	s_sub_i32 s17, s12, s2
	s_lshl_b32 s13, s17, 5
	s_lshl_b32 s3, s3, 4
	s_bfe_u32 s4, s17, 0x40009
	s_bfe_u32 s16, s17, 0x40005
	s_and_b32 s2, s13, 0x3e0
	s_ashr_i32 s15, s17, 13
	s_or_b32 s8, s4, s3
	s_cmp_gt_i32 s15, 1
	s_mov_b64 s[10:11], -1
	s_cbranch_scc0 .LBB0_1351
	s_ashr_i32 s9, s8, 31
	v_readlane_b32 s20, v253, 8
	s_lshl_b64 s[4:5], s[8:9], 22
	v_readlane_b32 s22, v253, 10
	v_readlane_b32 s23, v253, 11
	s_add_u32 s3, s22, s4
	s_addc_u32 s4, s23, s5
	s_lshl_b32 s30, s16, 6
	s_lshl_b32 s5, s16, 18
	s_add_u32 s5, s3, s5
	s_addc_u32 s4, s4, 0
	s_lshl_b32 s6, s2, 2
	s_add_u32 s6, s5, s6
	s_addc_u32 s7, s4, 0
	s_lshl_b64 s[4:5], s[8:9], 21
	s_add_u32 s4, s0, s4
	s_addc_u32 s5, s1, s5
	s_add_u32 s4, s4, 0x31a00000
	v_readlane_b32 s21, v253, 9
	v_readlane_b32 s24, v253, 12
	v_readlane_b32 s25, v253, 13
	v_readlane_b32 s26, v253, 14
	v_readlane_b32 s27, v253, 15
	s_mov_b32 s3, s31
	s_addc_u32 s5, s5, 0
	s_mov_b64 s[10:11], 0

.LBB0_1432:
	s_cmp_lg_u32 s1, 3
	v_readlane_b32 s2, v254, 39
	s_cselect_b64 s[0:1], -1, 0
	v_readlane_b32 s3, v254, 40
	s_and_b64 s[0:1], s[2:3], s[0:1]
	s_cmpk_gt_i32 s4, 0x7f
	s_cselect_b64 s[2:3], -1, 0
	s_and_b64 s[0:1], s[0:1], s[2:3]
	s_andn2_b64 vcc, exec, s[0:1]
	s_cbranch_vccnz .LBB0_1446
	v_readlane_b32 s0, v255, 1
	v_readlane_b32 s1, v255, 2
	s_and_b64 s[0:1], s[0:1], exec
	s_movk_i32 s0, 0xfc0
	v_readlane_b32 s2, v254, 59
	s_cselect_b32 s0, s0, 0x6c0
	s_cmp_eq_u32 s2, 0
	s_mov_b32 s1, 0x84a0
	s_cselect_b32 s1, 0x2e0, s1
	s_cmp_gt_u32 s2, 1
	s_cselect_b32 s2, 0x78c0, 0
	s_add_i32 s1, s1, s2
	s_add_i32 s14, s1, s0
	v_readlane_b32 s0, v255, 0
	s_mul_i32 s2, s0, 56
	s_add_i32 s3, s14, s56
	v_readlane_b32 s4, v253, 8
	s_add_i32 s12, s3, s2
	v_readlane_b32 s10, v253, 14
	v_readlane_b32 s11, v253, 15
	s_add_i32 s12, s12, 0x1600
	s_add_i32 s14, s14, 0x4e00
	s_min_u32 s14, s14, 0x18000
	s_mov_b64 s[0:1], s[10:11]
	s_cmp_ge_i32 s12, s14
	v_readlane_b32 s5, v253, 9
	v_readlane_b32 s6, v253, 10
	v_readlane_b32 s7, v253, 11
	v_readlane_b32 s8, v253, 12
	v_readlane_b32 s9, v253, 13
	v_mbcnt_lo_u32_b32 v0, -1, 0
	v_mbcnt_hi_u32_b32 v0, -1, v0
	s_cbranch_scc1 .LBB0_1446
	s_mul_hi_i32 s2, s12, 0x2aaaaaab
	s_lshr_b32 s3, s2, 31
	s_ashr_i32 s2, s2, 12
	s_add_i32 s3, s2, s3
	s_mul_i32 s2, s3, 0x6000
	s_sub_i32 s17, s12, s2
	s_lshl_b32 s13, s17, 5
	s_lshl_b32 s3, s3, 4
	s_bfe_u32 s4, s17, 0x40009
	s_bfe_u32 s16, s17, 0x40005
	s_and_b32 s2, s13, 0x3e0
	s_ashr_i32 s15, s17, 13
	s_or_b32 s8, s4, s3
	s_cmp_gt_i32 s15, 1
	s_mov_b64 s[10:11], -1
	s_cbranch_scc0 .LBB0_1436
	s_ashr_i32 s9, s8, 31
	v_readlane_b32 s20, v253, 8
	s_lshl_b64 s[4:5], s[8:9], 22
	v_readlane_b32 s22, v253, 10
	v_readlane_b32 s23, v253, 11
	s_add_u32 s3, s22, s4
	s_addc_u32 s4, s23, s5
	s_lshl_b32 s30, s16, 6
	s_lshl_b32 s5, s16, 18
	s_add_u32 s5, s3, s5
	s_addc_u32 s4, s4, 0
	s_lshl_b32 s6, s2, 2
	s_add_u32 s6, s5, s6
	s_addc_u32 s7, s4, 0
	s_lshl_b64 s[4:5], s[8:9], 21
	s_add_u32 s4, s0, s4
	s_addc_u32 s5, s1, s5
	s_add_u32 s4, s4, 0x31a00000
	v_readlane_b32 s21, v253, 9
	v_readlane_b32 s24, v253, 12
	v_readlane_b32 s25, v253, 13
	v_readlane_b32 s26, v253, 14
	v_readlane_b32 s27, v253, 15
	s_mov_b32 s3, s31
	s_addc_u32 s5, s5, 0
	s_mov_b64 s[10:11], 0

.LBB0_1513:
	s_cmp_lg_u32 s1, 3
	v_readlane_b32 s2, v254, 39
	s_cselect_b64 s[0:1], -1, 0
	v_readlane_b32 s3, v254, 40
	s_and_b64 s[0:1], s[2:3], s[0:1]
	s_cmp_gt_i32 s4, 63
	s_cselect_b64 s[2:3], -1, 0
	s_and_b64 s[0:1], s[0:1], s[2:3]
	s_andn2_b64 vcc, exec, s[0:1]
	s_cbranch_vccnz .LBB0_1527
	v_readlane_b32 s0, v255, 1
	v_readlane_b32 s1, v255, 2
	s_and_b64 s[0:1], s[0:1], exec
	s_movk_i32 s0, 0xfc0
	v_readlane_b32 s2, v254, 59
	s_cselect_b32 s0, s0, 0x6c0
	s_cmp_eq_u32 s2, 0
	s_mov_b32 s1, 0x84a0
	s_cselect_b32 s1, 0x2e0, s1
	s_cmp_gt_u32 s2, 1
	s_cselect_b32 s2, 0x78c0, 0
	s_add_i32 s1, s1, s2
	s_add_i32 s14, s1, s0
	s_mul_i32 s2, s4, 48
	s_add_i32 s3, s14, s56
	v_readlane_b32 s4, v253, 8
	s_add_i32 s12, s3, s2
	v_readlane_b32 s10, v253, 14
	v_readlane_b32 s11, v253, 15
	s_add_i32 s12, s12, 0x4200
	s_add_i32 s14, s14, 0x7200
	s_min_u32 s14, s14, 0x18000
	s_mov_b64 s[0:1], s[10:11]
	s_cmp_ge_i32 s12, s14
	v_readlane_b32 s5, v253, 9
	v_readlane_b32 s6, v253, 10
	v_readlane_b32 s7, v253, 11
	v_readlane_b32 s8, v253, 12
	v_readlane_b32 s9, v253, 13
	v_mbcnt_lo_u32_b32 v0, -1, 0
	v_mbcnt_hi_u32_b32 v0, -1, v0
	s_cbranch_scc1 .LBB0_1527
	s_mul_hi_i32 s2, s12, 0x2aaaaaab
	s_lshr_b32 s3, s2, 31
	s_ashr_i32 s2, s2, 12
	s_add_i32 s3, s2, s3
	s_mul_i32 s2, s3, 0x6000
	s_sub_i32 s17, s12, s2
	s_lshl_b32 s13, s17, 5
	s_lshl_b32 s3, s3, 4
	s_bfe_u32 s4, s17, 0x40009
	s_bfe_u32 s16, s17, 0x40005
	s_and_b32 s2, s13, 0x3e0
	s_ashr_i32 s15, s17, 13
	s_or_b32 s8, s4, s3
	s_cmp_gt_i32 s15, 1
	s_mov_b64 s[10:11], -1
	s_cbranch_scc0 .LBB0_1517
	s_ashr_i32 s9, s8, 31
	v_readlane_b32 s20, v253, 8
	s_lshl_b64 s[4:5], s[8:9], 22
	v_readlane_b32 s22, v253, 10
	v_readlane_b32 s23, v253, 11
	s_add_u32 s3, s22, s4
	s_addc_u32 s4, s23, s5
	s_lshl_b32 s30, s16, 6
	s_lshl_b32 s5, s16, 18
	s_add_u32 s5, s3, s5
	s_addc_u32 s4, s4, 0
	s_lshl_b32 s6, s2, 2
	s_add_u32 s6, s5, s6
	s_addc_u32 s7, s4, 0
	s_lshl_b64 s[4:5], s[8:9], 21
	s_add_u32 s4, s0, s4
	s_addc_u32 s5, s1, s5
	s_add_u32 s4, s4, 0x31a00000
	v_readlane_b32 s21, v253, 9
	v_readlane_b32 s24, v253, 12
	v_readlane_b32 s25, v253, 13
	v_readlane_b32 s26, v253, 14
	v_readlane_b32 s27, v253, 15
	s_mov_b32 s3, s31
	s_addc_u32 s5, s5, 0
	s_mov_b64 s[10:11], 0
